# v37 + MLA loop (issue-bound): 8 dead zero-inits and 10 canonicalising self-max per tile removed, one V address per tile, V reads hoisted, blanket lgkm waits dropped
# baseline (speedup 1.0000x reference)
.LBB0_565:
	s_waitcnt lgkmcnt(4)
	v_mfma_scale_f32_32x32x64_f8f6f4 v[96:111], v[96:103], v[120:127], 0, v205, v205 op_sel_hi:[0,0,0]
	v_cndmask_b32_e64 v176, v189, v192, s[4:5]
	v_fma_f32 v80, v80, s40, -v176
	v_fma_f32 v81, v81, s40, -v176
	v_fma_f32 v84, v84, s40, -v176
	v_fma_f32 v85, v85, s40, -v176
	v_fma_f32 v88, v88, s40, -v176
	v_fma_f32 v89, v89, s40, -v176
	v_fma_f32 v92, v92, s40, -v176
	v_fma_f32 v93, v93, s40, -v176
	v_exp_f32_e32 v80, v80
	v_exp_f32_e32 v81, v81
	v_exp_f32_e32 v84, v84
	v_exp_f32_e32 v85, v85
	v_exp_f32_e32 v88, v88
	v_exp_f32_e32 v89, v89
	s_waitcnt lgkmcnt(2)
	v_mfma_scale_f32_32x32x64_f8f6f4 v[96:111], v[156:163], v[128:135], v[96:111], v205, v205 op_sel_hi:[0,0,0]
	v_exp_f32_e32 v92, v92
	v_exp_f32_e32 v93, v93
	v_fma_f32 v82, v82, s40, -v176
	v_fma_f32 v83, v83, s40, -v176
	v_fma_f32 v86, v86, s40, -v176
	v_fma_f32 v87, v87, s40, -v176
	v_fma_f32 v90, v90, s40, -v176
	v_fma_f32 v91, v91, s40, -v176
	v_fma_f32 v94, v94, s40, -v176
	v_fma_f32 v95, v95, s40, -v176
	v_exp_f32_e32 v82, v82
	v_exp_f32_e32 v83, v83
	v_exp_f32_e32 v86, v86
	v_exp_f32_e32 v87, v87
	v_exp_f32_e32 v90, v90
	s_waitcnt lgkmcnt(0)
	v_mfma_scale_f32_32x32x64_f8f6f4 v[96:111], v[148:155], v[136:143], v[96:111], v205, v205 op_sel_hi:[0,0,0]
	v_lshl_add_u32 v240, s23, 14, v211
	ds_read_b128 v[224:227], v240
	ds_read_b128 v[228:231], v240 offset:16
	ds_read_b128 v[232:235], v240 offset:2560
	ds_read_b128 v[236:239], v240 offset:2576
	v_exp_f32_e32 v91, v91
	v_exp_f32_e32 v94, v94
	v_exp_f32_e32 v95, v95
	v_cvt_pk_fp8_f32 v148, v80, v81
	v_cvt_pk_fp8_f32 v149, v84, v85
	v_cvt_pk_fp8_f32 v150, v88, v89
	v_cvt_pk_fp8_f32 v151, v92, v93
	v_cvt_pk_fp8_f32 v148, v82, v83 op_sel:[0,0,1]
	v_cvt_pk_fp8_f32 v149, v86, v87 op_sel:[0,0,1]
	v_cvt_pk_fp8_f32 v150, v90, v91 op_sel:[0,0,1]
	v_cvt_pk_fp8_f32 v151, v94, v95 op_sel:[0,0,1]
	s_nop 0
	s_waitcnt lgkmcnt(2)
	v_mfma_scale_f32_32x32x64_f8f6f4 v[48:63], v[144:151], v[224:231], v[48:63], v205, v205 op_sel_hi:[0,0,0]
	ds_read_b128 v[80:83], v240 offset:5120
	ds_read_b128 v[84:87], v240 offset:5136
	ds_read_b128 v[152:155], v240 offset:7680
	ds_read_b128 v[156:159], v240 offset:7696
	s_waitcnt lgkmcnt(4)
	v_mfma_scale_f32_32x32x64_f8f6f4 v[32:47], v[144:151], v[232:239], v[32:47], v205, v205 op_sel_hi:[0,0,0]
	v_max_f32_e32 v88, v96, v97
	v_max3_f32 v88, v88, v98, v99
	v_max3_f32 v88, v88, v100, v101
	v_max3_f32 v88, v88, v102, v103
	v_max3_f32 v88, v88, v104, v105
	v_max3_f32 v88, v88, v106, v107
	s_waitcnt lgkmcnt(2)
	v_mfma_scale_f32_32x32x64_f8f6f4 v[16:31], v[144:151], v[80:87], v[16:31], v205, v205 op_sel_hi:[0,0,0]
	v_max3_f32 v88, v88, v108, v109
	v_max3_f32 v88, v88, v110, v111
	v_mov_b32_e32 v89, v88
	s_nop 1
	v_permlane32_swap_b32_e32 v88, v89
	v_max_f32_e32 v80, v88, v89
	v_fma_f32 v81, v80, s40, -v176
	v_cmp_ge_f32_e32 vcc, s70, v81
	v_fmamk_f32 v80, v80, 0x3dd53b94, v202
	v_max_f32_e32 v80, v176, v80
	v_sub_f32_e32 v81, v176, v80
	v_exp_f32_e32 v81, v81
	s_waitcnt lgkmcnt(0)
	v_mfma_scale_f32_32x32x64_f8f6f4 v[0:15], v[144:151], v[152:159], v[0:15], v205, v205 op_sel_hi:[0,0,0]
	s_cmp_eq_u64 vcc, exec
	s_cselect_b64 vcc, -1, 0
	v_cndmask_b32_e32 v192, v80, v176, vcc
	s_add_i32 s21, s21, 2
	s_add_i32 s78, s78, 1
	s_add_i32 s22, s22, 64
	v_fma_f32 v178, v96, s40, -v192
	v_fma_f32 v179, v97, s40, -v192
	v_fma_f32 v176, v98, s40, -v192
	v_fma_f32 v177, v99, s40, -v192
	v_fma_f32 v162, v100, s40, -v192
	v_fma_f32 v163, v101, s40, -v192
	v_fma_f32 v160, v102, s40, -v192
	v_fma_f32 v161, v103, s40, -v192
	v_pk_fma_f32 v[158:159], v[104:105], s[40:41], v[192:193] op_sel_hi:[1,0,0] neg_lo:[0,0,1] neg_hi:[0,0,1]
	v_pk_fma_f32 v[156:157], v[106:107], s[40:41], v[192:193] op_sel_hi:[1,0,0] neg_lo:[0,0,1] neg_hi:[0,0,1]
	v_pk_fma_f32 v[154:155], v[108:109], s[40:41], v[192:193] op_sel_hi:[1,0,0] neg_lo:[0,0,1] neg_hi:[0,0,1]
	v_pk_fma_f32 v[152:153], v[110:111], s[40:41], v[192:193] op_sel_hi:[1,0,0] neg_lo:[0,0,1] neg_hi:[0,0,1]
	v_cndmask_b32_e64 v88, v81, 1.0, vcc
	v_mfma_scale_f32_32x32x64_f8f6f4 v[64:79], v[144:151], v[112:119], v[64:79], v205, v205 op_sel_hi:[0,0,0]
	s_cmp_ge_u32 s21, s17
	s_barrier
	s_cbranch_scc1 .LBB0_580

.LBB0_570:
	s_waitcnt lgkmcnt(4)
	v_mfma_scale_f32_32x32x64_f8f6f4 v[80:95], v[80:87], v[120:127], 0, v205, v205 op_sel_hi:[0,0,0]
	s_mov_b64 s[4:5], exec
	s_cmp_ge_u32 s18, s20
	s_waitcnt lgkmcnt(2)
	v_mfma_scale_f32_32x32x64_f8f6f4 v[80:95], v[104:111], v[128:135], v[80:95], v205, v205 op_sel_hi:[0,0,0]
	s_waitcnt lgkmcnt(0)
	v_mfma_scale_f32_32x32x64_f8f6f4 v[80:95], v[96:103], v[136:143], v[80:95], v205, v205 op_sel_hi:[0,0,0]
	s_nop 15
	s_nop 3
	v_max_f32_e32 v96, v80, v81
	v_max3_f32 v96, v96, v82, v83
	v_max3_f32 v96, v96, v84, v85
	v_max3_f32 v96, v96, v86, v87
	v_max3_f32 v96, v96, v88, v89
	v_max3_f32 v96, v96, v90, v91
	v_max3_f32 v96, v96, v92, v93
	v_max3_f32 v96, v96, v94, v95
	v_mov_b32_e32 v97, v96
	s_nop 1
	v_permlane32_swap_b32_e32 v96, v97
	v_max_f32_e32 v96, v96, v97
	v_fma_f32 v97, v96, s40, -v192
	v_cmp_ge_f32_e32 vcc, s70, v97
	s_cbranch_scc1 .LBB0_577
	s_xor_b32 s25, s23, 1
	s_lshl_b32 s18, s25, 15
	s_add_i32 s26, s18, 0
	v_add3_u32 v97, s26, v212, v190
	s_waitcnt vmcnt(1)
	ds_write_b128 v97, v[168:171]
	s_and_saveexec_b64 s[18:19], s[0:1]
	v_add3_u32 v97, s26, v215, v188
	ds_write_b128 v97, v[164:167]
	s_or_b64 exec, exec, s[18:19]
	v_lshl_add_u32 v97, s25, 14, v207
	s_cmp_ge_u32 s78, s74
	s_waitcnt vmcnt(0)
	ds_write_b128 v97, v[172:175]
	s_cbranch_scc1 .LBB0_577
	s_cmp_lt_u32 s78, s77
	s_cselect_b32 s18, 0, s77
	s_cselect_b32 s19, s76, s75
	s_lshl_b32 s18, s18, 6
	s_sub_i32 s25, s19, s18
	s_add_i32 s25, s25, s22
	v_add_u32_e32 v97, s25, v210
	v_mad_i64_i32 v[98:99], s[18:19], v97, s64, v[194:195]
	global_load_dwordx4 v[168:171], v[98:99], off
	s_and_saveexec_b64 s[18:19], s[0:1]
	s_cbranch_execz .LBB0_576
	v_add_u32_e32 v97, s25, v213
	v_mad_i64_i32 v[98:99], s[26:27], v97, s64, v[196:197]
	global_load_dwordx4 v[164:167], v[98:99], off

.LBB0_577:
	v_mul_f32_e32 v96, 0x3dd53b94, v96
	v_add_f32_e32 v96, 0xc0a00000, v96
	v_max_f32_e32 v189, v192, v96
	v_sub_f32_e32 v96, v192, v189
	v_exp_f32_e32 v96, v96
	s_cmp_eq_u64 vcc, s[4:5]
	s_cselect_b64 s[4:5], -1, 0
	v_exp_f32_e32 v97, v179
	v_cndmask_b32_e64 v191, v96, 1.0, s[4:5]
	v_exp_f32_e32 v96, v178
	v_exp_f32_e32 v100, v162
	v_exp_f32_e32 v101, v163
	v_exp_f32_e32 v104, v158
	v_exp_f32_e32 v105, v159
	v_exp_f32_e32 v108, v154
	v_exp_f32_e32 v109, v155
	v_exp_f32_e32 v98, v176
	v_exp_f32_e32 v99, v177
	v_exp_f32_e32 v102, v160
	v_exp_f32_e32 v103, v161
	v_cvt_pk_fp8_f32 v144, v96, v97
	v_cvt_pk_fp8_f32 v145, v100, v101
	s_xor_b32 s18, s24, 0x8000
	v_exp_f32_e32 v106, v156
	v_exp_f32_e32 v107, v157
	v_exp_f32_e32 v110, v152
	v_cvt_pk_fp8_f32 v146, v104, v105
	v_exp_f32_e32 v104, v153
	v_cvt_pk_fp8_f32 v147, v108, v109
	v_add_u32_e32 v105, s18, v216
	v_cvt_pk_fp8_f32 v144, v98, v99 op_sel:[0,0,1]
	v_cvt_pk_fp8_f32 v145, v102, v103 op_sel:[0,0,1]
	s_waitcnt lgkmcnt(0)
	s_barrier
	ds_read_b128 v[96:99], v105
	ds_read_b128 v[100:103], v105 offset:16
	ds_read_b128 v[156:159], v105 offset:64
	ds_read_b128 v[160:163], v105 offset:80
	v_add_u32_e32 v105, v105, v217
	ds_read_b128 v[148:151], v105 offset:128
	ds_read_b128 v[152:155], v105 offset:160
	v_cvt_pk_fp8_f32 v146, v106, v107 op_sel:[0,0,1]
	v_cvt_pk_fp8_f32 v147, v110, v104 op_sel:[0,0,1]
	v_cmp_gt_f32_e32 vcc, 1.0, v191
	s_cbranch_vccz .LBB0_565
	s_and_saveexec_b64 s[18:19], s[2:3]
	s_cbranch_execz .LBB0_564
	ds_write_b32 v209, v191 offset:128
	s_branch .LBB0_564

.LBB0_1875:
	s_waitcnt lgkmcnt(4)
	v_mfma_scale_f32_32x32x64_f8f6f4 v[96:111], v[96:103], v[120:127], 0, v207, v207 op_sel_hi:[0,0,0]
	v_cndmask_b32_e64 v176, v191, v194, s[4:5]
	v_fma_f32 v80, v80, s38, -v176
	v_fma_f32 v81, v81, s38, -v176
	v_fma_f32 v84, v84, s38, -v176
	v_fma_f32 v85, v85, s38, -v176
	v_fma_f32 v88, v88, s38, -v176
	v_fma_f32 v89, v89, s38, -v176
	v_fma_f32 v92, v92, s38, -v176
	v_fma_f32 v93, v93, s38, -v176
	v_exp_f32_e32 v80, v80
	v_exp_f32_e32 v81, v81
	v_exp_f32_e32 v84, v84
	v_exp_f32_e32 v85, v85
	v_exp_f32_e32 v88, v88
	v_exp_f32_e32 v89, v89
	s_waitcnt lgkmcnt(2)
	v_mfma_scale_f32_32x32x64_f8f6f4 v[96:111], v[156:163], v[128:135], v[96:111], v207, v207 op_sel_hi:[0,0,0]
	v_exp_f32_e32 v92, v92
	v_exp_f32_e32 v93, v93
	v_fma_f32 v82, v82, s38, -v176
	v_fma_f32 v83, v83, s38, -v176
	v_fma_f32 v86, v86, s38, -v176
	v_fma_f32 v87, v87, s38, -v176
	v_fma_f32 v90, v90, s38, -v176
	v_fma_f32 v91, v91, s38, -v176
	v_fma_f32 v94, v94, s38, -v176
	v_fma_f32 v95, v95, s38, -v176
	v_exp_f32_e32 v82, v82
	v_exp_f32_e32 v83, v83
	v_exp_f32_e32 v86, v86
	v_exp_f32_e32 v87, v87
	v_exp_f32_e32 v90, v90
	s_waitcnt lgkmcnt(0)
	v_mfma_scale_f32_32x32x64_f8f6f4 v[96:111], v[148:155], v[136:143], v[96:111], v207, v207 op_sel_hi:[0,0,0]
	v_lshl_add_u32 v240, s24, 14, v209
	ds_read_b128 v[224:227], v240
	ds_read_b128 v[228:231], v240 offset:16
	ds_read_b128 v[232:235], v240 offset:2560
	ds_read_b128 v[236:239], v240 offset:2576
	v_exp_f32_e32 v91, v91
	v_exp_f32_e32 v94, v94
	v_exp_f32_e32 v95, v95
	v_cvt_pk_fp8_f32 v148, v80, v81
	v_cvt_pk_fp8_f32 v149, v84, v85
	v_cvt_pk_fp8_f32 v150, v88, v89
	v_cvt_pk_fp8_f32 v151, v92, v93
	v_cvt_pk_fp8_f32 v148, v82, v83 op_sel:[0,0,1]
	v_cvt_pk_fp8_f32 v149, v86, v87 op_sel:[0,0,1]
	v_cvt_pk_fp8_f32 v150, v90, v91 op_sel:[0,0,1]
	v_cvt_pk_fp8_f32 v151, v94, v95 op_sel:[0,0,1]
	s_nop 0
	s_waitcnt lgkmcnt(2)
	v_mfma_scale_f32_32x32x64_f8f6f4 v[48:63], v[144:151], v[224:231], v[48:63], v207, v207 op_sel_hi:[0,0,0]
	ds_read_b128 v[80:83], v240 offset:5120
	ds_read_b128 v[84:87], v240 offset:5136
	ds_read_b128 v[152:155], v240 offset:7680
	ds_read_b128 v[156:159], v240 offset:7696
	s_waitcnt lgkmcnt(4)
	v_mfma_scale_f32_32x32x64_f8f6f4 v[32:47], v[144:151], v[232:239], v[32:47], v207, v207 op_sel_hi:[0,0,0]
	v_max_f32_e32 v88, v96, v97
	v_max3_f32 v88, v88, v98, v99
	v_max3_f32 v88, v88, v100, v101
	v_max3_f32 v88, v88, v102, v103
	v_max3_f32 v88, v88, v104, v105
	v_max3_f32 v88, v88, v106, v107
	s_waitcnt lgkmcnt(2)
	v_mfma_scale_f32_32x32x64_f8f6f4 v[16:31], v[144:151], v[80:87], v[16:31], v207, v207 op_sel_hi:[0,0,0]
	v_max3_f32 v88, v88, v108, v109
	v_max3_f32 v88, v88, v110, v111
	v_mov_b32_e32 v89, v88
	s_nop 1
	v_permlane32_swap_b32_e32 v88, v89
	v_max_f32_e32 v80, v88, v89
	v_fma_f32 v81, v80, s38, -v176
	v_cmp_ge_f32_e32 vcc, s68, v81
	v_fmamk_f32 v80, v80, 0x3dd53b94, v204
	v_max_f32_e32 v80, v176, v80
	v_sub_f32_e32 v81, v176, v80
	v_exp_f32_e32 v81, v81
	s_waitcnt lgkmcnt(0)
	v_mfma_scale_f32_32x32x64_f8f6f4 v[0:15], v[144:151], v[152:159], v[0:15], v207, v207 op_sel_hi:[0,0,0]
	s_cmp_eq_u64 vcc, exec
	s_cselect_b64 vcc, -1, 0
	v_cndmask_b32_e32 v194, v80, v176, vcc
	v_fma_f32 v178, v96, s38, -v194
	v_fma_f32 v179, v97, s38, -v194
	v_fma_f32 v176, v98, s38, -v194
	v_fma_f32 v177, v99, s38, -v194
	v_fma_f32 v162, v100, s38, -v194
	v_fma_f32 v163, v101, s38, -v194
	v_fma_f32 v160, v102, s38, -v194
	v_fma_f32 v161, v103, s38, -v194
	v_fma_f32 v158, v104, s38, -v194
	v_fma_f32 v159, v105, s38, -v194
	v_pk_fma_f32 v[156:157], v[106:107], s[38:39], v[194:195] op_sel_hi:[1,0,0] neg_lo:[0,0,1] neg_hi:[0,0,1]
	v_pk_fma_f32 v[154:155], v[108:109], s[38:39], v[194:195] op_sel_hi:[1,0,0] neg_lo:[0,0,1] neg_hi:[0,0,1]
	v_pk_fma_f32 v[152:153], v[110:111], s[38:39], v[194:195] op_sel_hi:[1,0,0] neg_lo:[0,0,1] neg_hi:[0,0,1]
	v_cndmask_b32_e64 v88, v81, 1.0, vcc
	s_add_i32 s17, s17, 2
	s_add_i32 s76, s76, 1
	s_and_b64 vcc, exec, s[18:19]
	v_mfma_scale_f32_32x32x64_f8f6f4 v[64:79], v[144:151], v[112:119], v[64:79], v207, v207 op_sel_hi:[0,0,0]
	s_barrier
	s_cbranch_vccnz .LBB0_1889

.LBB0_1880:
	s_waitcnt lgkmcnt(4)
	v_mfma_scale_f32_32x32x64_f8f6f4 v[80:95], v[80:87], v[120:127], 0, v207, v207 op_sel_hi:[0,0,0]
	s_xor_b32 s22, s24, 1
	s_lshl_b32 s18, s22, 15
	s_add_i32 s23, s18, 0
	s_mov_b64 s[20:21], exec
	s_waitcnt lgkmcnt(2)
	v_mfma_scale_f32_32x32x64_f8f6f4 v[80:95], v[104:111], v[128:135], v[80:95], v207, v207 op_sel_hi:[0,0,0]
	s_waitcnt lgkmcnt(0)
	v_mfma_scale_f32_32x32x64_f8f6f4 v[80:95], v[96:103], v[136:143], v[80:95], v207, v207 op_sel_hi:[0,0,0]
	s_nop 15
	s_nop 3
	v_max_f32_e32 v96, v80, v81
	v_max3_f32 v96, v96, v82, v83
	v_max3_f32 v96, v96, v84, v85
	v_max3_f32 v96, v96, v86, v87
	v_max3_f32 v96, v96, v88, v89
	v_max3_f32 v96, v96, v90, v91
	v_max3_f32 v96, v96, v92, v93
	v_max3_f32 v96, v96, v94, v95
	v_mov_b32_e32 v97, v96
	s_nop 1
	v_permlane32_swap_b32_e32 v96, v97
	v_max_f32_e32 v96, v96, v97
	v_fma_f32 v97, v96, s38, -v194
	v_cmp_ge_f32_e64 s[4:5], s68, v97
	v_add3_u32 v97, s23, v210, v190
	s_waitcnt vmcnt(1)
	ds_write_b128 v97, v[168:171]
	s_and_saveexec_b64 s[18:19], s[0:1]
	v_add3_u32 v97, s23, v216, v192
	ds_write_b128 v97, v[164:167]
	s_or_b64 exec, exec, s[18:19]
	s_cmpk_gt_u32 s17, 0x83
	s_cselect_b64 s[18:19], -1, 0
	v_lshl_add_u32 v97, s22, 14, v211
	s_and_b64 vcc, exec, s[18:19]
	s_waitcnt vmcnt(0)
	ds_write_b128 v97, v[172:175]
	s_cbranch_vccnz .LBB0_1886
	s_cmpk_lt_u32 s17, 0x7c
	s_cselect_b32 s22, 0, 0xffffffc0
	s_cselect_b32 s23, s74, s75
	s_add_i32 s22, s22, s76
	s_lshl_b32 s26, s22, 6
	s_add_i32 s26, s26, s23
	v_add_u32_e32 v97, s26, v189
	v_mad_i64_i32 v[98:99], s[22:23], v97, s62, v[196:197]
	global_load_dwordx4 v[168:171], v[98:99], off
	s_and_saveexec_b64 s[22:23], s[0:1]
	s_cbranch_execz .LBB0_1885
	v_add_u32_e32 v97, s26, v212
	v_mad_i64_i32 v[98:99], s[28:29], v97, s62, v[198:199]
	global_load_dwordx4 v[164:167], v[98:99], off

.LBB0_1886:
	v_mul_f32_e32 v96, 0x3dd53b94, v96
	v_add_f32_e32 v96, 0xc0a00000, v96
	v_max_f32_e32 v191, v194, v96
	v_sub_f32_e32 v96, v194, v191
	v_exp_f32_e32 v96, v96
	s_cmp_eq_u64 s[4:5], s[20:21]
	s_cselect_b64 s[4:5], -1, 0
	v_exp_f32_e32 v97, v179
	v_cndmask_b32_e64 v193, v96, 1.0, s[4:5]
	v_exp_f32_e32 v96, v178
	v_exp_f32_e32 v100, v162
	v_exp_f32_e32 v101, v163
	v_exp_f32_e32 v104, v158
	v_exp_f32_e32 v105, v159
	v_exp_f32_e32 v108, v154
	v_exp_f32_e32 v109, v155
	v_exp_f32_e32 v98, v176
	v_exp_f32_e32 v99, v177
	v_exp_f32_e32 v102, v160
	v_exp_f32_e32 v103, v161
	v_cvt_pk_fp8_f32 v144, v96, v97
	v_cvt_pk_fp8_f32 v145, v100, v101
	s_xor_b32 s20, s25, 0x8000
	v_exp_f32_e32 v106, v156
	v_exp_f32_e32 v107, v157
	v_exp_f32_e32 v110, v152
	v_cvt_pk_fp8_f32 v146, v104, v105
	v_exp_f32_e32 v104, v153
	v_cvt_pk_fp8_f32 v147, v108, v109
	v_add_u32_e32 v105, s20, v214
	v_cvt_pk_fp8_f32 v144, v98, v99 op_sel:[0,0,1]
	v_cvt_pk_fp8_f32 v145, v102, v103 op_sel:[0,0,1]
	s_waitcnt lgkmcnt(0)
	s_barrier
	ds_read_b128 v[96:99], v105
	ds_read_b128 v[100:103], v105 offset:16
	ds_read_b128 v[156:159], v105 offset:64
	ds_read_b128 v[160:163], v105 offset:80
	v_add_u32_e32 v105, v105, v215
	ds_read_b128 v[148:151], v105 offset:128
	ds_read_b128 v[152:155], v105 offset:160
	v_cvt_pk_fp8_f32 v146, v106, v107 op_sel:[0,0,1]
	v_cvt_pk_fp8_f32 v147, v110, v104 op_sel:[0,0,1]
	v_cmp_gt_f32_e32 vcc, 1.0, v193
	s_cbranch_vccz .LBB0_1875
	s_and_saveexec_b64 s[20:21], s[2:3]
	s_cbranch_execz .LBB0_1874
	ds_write_b32 v208, v193 offset:128
	s_branch .LBB0_1874
